# P6 wide LN1 stores with sc0 sc1 write-through (as on the P9 row stores)
# speedup vs baseline: 1.0065x; 1.0006x over previous
.LBB0_706:
	v_lshl_add_u64 v[8:9], s[92:93], 0, v[4:5]
	v_add_co_u32_e32 v10, vcc, 0x69400000, v8
	v_mov_b32_e32 v144, 0
	s_nop 0
	v_addc_co_u32_e32 v11, vcc, 0, v9, vcc
	v_add_co_u32_e32 v8, vcc, s43, v8
	v_lshl_add_u32 v144, v144, 2, v132
	s_nop 0
	v_addc_co_u32_e32 v9, vcc, 0, v9, vcc
	s_waitcnt vmcnt(4)
	v_lshlrev_b32_e32 v6, 16, v160
	v_and_b32_e32 v7, 0xffff0000, v160
	v_lshlrev_b32_e32 v70, 16, v161
	v_and_b32_e32 v71, 0xffff0000, v161
	v_add_f32_e32 v12, v6, v7
	v_add_f32_e32 v13, v70, v71
	v_add_f32_e32 v12, v12, v13
	v_add_f32_e32 v14, 0, v12
	v_lshlrev_b32_e32 v66, 16, v162
	v_and_b32_e32 v67, 0xffff0000, v162
	v_lshlrev_b32_e32 v68, 16, v163
	v_and_b32_e32 v69, 0xffff0000, v163
	v_add_f32_e32 v12, v66, v67
	v_add_f32_e32 v13, v68, v69
	v_add_f32_e32 v12, v12, v13
	v_add_f32_e32 v14, v14, v12
	v_lshlrev_b32_e32 v64, 16, v164
	v_and_b32_e32 v65, 0xffff0000, v164
	v_lshlrev_b32_e32 v62, 16, v165
	v_and_b32_e32 v63, 0xffff0000, v165
	v_add_f32_e32 v12, v64, v65
	v_add_f32_e32 v13, v62, v63
	v_add_f32_e32 v12, v12, v13
	v_add_f32_e32 v14, v14, v12
	v_lshlrev_b32_e32 v58, 16, v166
	v_and_b32_e32 v59, 0xffff0000, v166
	v_lshlrev_b32_e32 v60, 16, v167
	v_and_b32_e32 v61, 0xffff0000, v167
	v_add_f32_e32 v12, v58, v59
	v_add_f32_e32 v13, v60, v61
	v_add_f32_e32 v12, v12, v13
	v_add_f32_e32 v14, v14, v12
	v_lshlrev_b32_e32 v56, 16, v168
	v_and_b32_e32 v57, 0xffff0000, v168
	v_lshlrev_b32_e32 v54, 16, v169
	v_and_b32_e32 v55, 0xffff0000, v169
	v_add_f32_e32 v12, v56, v57
	v_add_f32_e32 v13, v54, v55
	v_add_f32_e32 v12, v12, v13
	v_add_f32_e32 v14, v14, v12
	v_lshlrev_b32_e32 v32, 16, v170
	v_and_b32_e32 v33, 0xffff0000, v170
	v_lshlrev_b32_e32 v52, 16, v171
	v_and_b32_e32 v53, 0xffff0000, v171
	v_add_f32_e32 v12, v32, v33
	v_add_f32_e32 v13, v52, v53
	v_add_f32_e32 v12, v12, v13
	v_add_f32_e32 v14, v14, v12
	v_lshlrev_b32_e32 v30, 16, v172
	v_and_b32_e32 v31, 0xffff0000, v172
	v_lshlrev_b32_e32 v28, 16, v173
	v_and_b32_e32 v29, 0xffff0000, v173
	v_add_f32_e32 v12, v30, v31
	v_add_f32_e32 v13, v28, v29
	v_add_f32_e32 v12, v12, v13
	v_add_f32_e32 v12, v14, v12
	v_lshlrev_b32_e32 v24, 16, v174
	v_and_b32_e32 v25, 0xffff0000, v174
	v_lshlrev_b32_e32 v26, 16, v175
	v_and_b32_e32 v27, 0xffff0000, v175
	v_add_f32_e32 v10, v24, v25
	v_add_f32_e32 v11, v26, v27
	v_add_f32_e32 v10, v10, v11
	v_add_f32_e32 v34, v12, v10
	global_load_dwordx2 v[22:23], v[8:9], off
	global_load_dwordx2 v[20:21], v[8:9], off offset:512
	global_load_dwordx2 v[18:19], v[8:9], off offset:1024
	global_load_dwordx2 v[16:17], v[8:9], off offset:1536
	global_load_dwordx2 v[14:15], v[8:9], off offset:2048
	global_load_dwordx2 v[12:13], v[8:9], off offset:2560
	global_load_dwordx2 v[10:11], v[8:9], off offset:3072
	s_nop 0
	global_load_dwordx2 v[8:9], v[8:9], off offset:3584
	s_cmp_lt_i32 s36, 4
	s_cselect_b32 s12, s30, 0
	s_cselect_b32 s13, s31, 0
	v_lshl_add_u64 v[176:177], v[4:5], 0, s[12:13]
	v_lshl_add_u64 v[176:177], s[92:93], 0, v[176:177]
	s_mov_b32 s12, 0x69400000
	s_mov_b32 s13, 0
	v_lshl_add_u64 v[176:177], v[176:177], 0, s[12:13]
	global_load_dwordx2 v[160:161], v[176:177], off
	global_load_dwordx2 v[162:163], v[176:177], off offset:512
	global_load_dwordx2 v[164:165], v[176:177], off offset:1024
	global_load_dwordx2 v[166:167], v[176:177], off offset:1536
	global_load_dwordx2 v[168:169], v[176:177], off offset:2048
	global_load_dwordx2 v[170:171], v[176:177], off offset:2560
	global_load_dwordx2 v[172:173], v[176:177], off offset:3072
	global_load_dwordx2 v[174:175], v[176:177], off offset:3584
	v_add_f32_dpp v34, v34, v34 quad_perm:[1,0,3,2] row_mask:0xf bank_mask:0xf bound_ctrl:1
	s_nop 1
	v_add_f32_dpp v34, v34, v34 quad_perm:[2,3,0,1] row_mask:0xf bank_mask:0xf bound_ctrl:1
	s_nop 1
	v_add_f32_dpp v34, v34, v34 row_half_mirror row_mask:0xf bank_mask:0xf bound_ctrl:1
	s_nop 1
	v_add_f32_dpp v34, v34, v34 row_mirror row_mask:0xf bank_mask:0xf bound_ctrl:1
	v_mov_b32_e32 v145, v34
	s_nop 1
	v_permlane16_swap_b32_e32 v34, v145
	v_add_f32_e32 v34, v34, v145
	v_mov_b32_e32 v145, v34
	s_nop 1
	v_permlane32_swap_b32_e32 v34, v145
	v_add_f32_e32 v145, v34, v145
	v_fmac_f32_e32 v71, 0xba000000, v145
	v_fmac_f32_e32 v7, 0xba000000, v145
	v_fmac_f32_e32 v70, 0xba000000, v145
	v_fmac_f32_e32 v6, 0xba000000, v145
	v_mul_f32_e32 v34, v7, v7
	v_mul_f32_e32 v146, v71, v71
	v_fmac_f32_e32 v34, v6, v6
	v_fmac_f32_e32 v146, v70, v70
	v_fmac_f32_e32 v69, 0xba000000, v145
	v_fmac_f32_e32 v67, 0xba000000, v145
	v_add_f32_e32 v34, v34, v146
	v_fmac_f32_e32 v68, 0xba000000, v145
	v_fmac_f32_e32 v66, 0xba000000, v145
	v_mul_f32_e32 v146, v67, v67
	v_mul_f32_e32 v147, v69, v69
	v_fmac_f32_e32 v146, v66, v66
	v_fmac_f32_e32 v147, v68, v68
	v_add_f32_e32 v146, v146, v147
	v_fmac_f32_e32 v63, 0xba000000, v145
	v_fmac_f32_e32 v65, 0xba000000, v145
	v_add_f32_e32 v34, v34, v146
	v_fmac_f32_e32 v62, 0xba000000, v145
	v_fmac_f32_e32 v64, 0xba000000, v145
	v_mul_f32_e32 v146, v65, v65
	v_mul_f32_e32 v147, v63, v63
	v_fmac_f32_e32 v146, v64, v64
	v_fmac_f32_e32 v147, v62, v62
	v_add_f32_e32 v146, v146, v147
	v_fmac_f32_e32 v61, 0xba000000, v145
	v_fmac_f32_e32 v59, 0xba000000, v145
	v_add_f32_e32 v34, v146, v34
	v_fmac_f32_e32 v60, 0xba000000, v145
	v_fmac_f32_e32 v58, 0xba000000, v145
	v_mul_f32_e32 v146, v59, v59
	v_mul_f32_e32 v147, v61, v61
	v_fmac_f32_e32 v146, v58, v58
	v_fmac_f32_e32 v147, v60, v60
	v_add_f32_e32 v146, v146, v147
	v_fmac_f32_e32 v55, 0xba000000, v145
	v_fmac_f32_e32 v57, 0xba000000, v145
	v_add_f32_e32 v34, v146, v34
	v_fmac_f32_e32 v54, 0xba000000, v145
	v_fmac_f32_e32 v56, 0xba000000, v145
	v_mul_f32_e32 v146, v57, v57
	v_mul_f32_e32 v147, v55, v55
	v_fmac_f32_e32 v146, v56, v56
	v_fmac_f32_e32 v147, v54, v54
	v_add_f32_e32 v146, v146, v147
	v_fmac_f32_e32 v53, 0xba000000, v145
	v_fmac_f32_e32 v33, 0xba000000, v145
	v_add_f32_e32 v34, v146, v34
	v_fmac_f32_e32 v52, 0xba000000, v145
	v_fmac_f32_e32 v32, 0xba000000, v145
	v_mul_f32_e32 v146, v33, v33
	v_mul_f32_e32 v147, v53, v53
	v_fmac_f32_e32 v146, v32, v32
	v_fmac_f32_e32 v147, v52, v52
	v_add_f32_e32 v146, v146, v147
	v_fmac_f32_e32 v29, 0xba000000, v145
	v_fmac_f32_e32 v31, 0xba000000, v145
	v_add_f32_e32 v34, v146, v34
	v_fmac_f32_e32 v28, 0xba000000, v145
	v_fmac_f32_e32 v30, 0xba000000, v145
	v_mul_f32_e32 v146, v31, v31
	v_mul_f32_e32 v147, v29, v29
	v_fmac_f32_e32 v146, v30, v30
	v_fmac_f32_e32 v147, v28, v28
	v_add_f32_e32 v146, v146, v147
	v_fmac_f32_e32 v27, 0xba000000, v145
	v_fmac_f32_e32 v25, 0xba000000, v145
	v_add_f32_e32 v34, v146, v34
	v_fmac_f32_e32 v26, 0xba000000, v145
	v_fmac_f32_e32 v24, 0xba000000, v145
	v_mul_f32_e32 v146, v25, v25
	v_mul_f32_e32 v147, v27, v27
	v_fmac_f32_e32 v146, v24, v24
	v_fmac_f32_e32 v147, v26, v26
	v_add_f32_e32 v146, v146, v147
	v_add_f32_e32 v34, v146, v34
	s_nop 1
	v_add_f32_dpp v34, v34, v34 quad_perm:[1,0,3,2] row_mask:0xf bank_mask:0xf bound_ctrl:1
	s_nop 1
	v_add_f32_dpp v34, v34, v34 quad_perm:[2,3,0,1] row_mask:0xf bank_mask:0xf bound_ctrl:1
	s_nop 1
	v_add_f32_dpp v34, v34, v34 row_half_mirror row_mask:0xf bank_mask:0xf bound_ctrl:1
	s_nop 1
	v_add_f32_dpp v34, v34, v34 row_mirror row_mask:0xf bank_mask:0xf bound_ctrl:1
	v_mov_b32_e32 v146, v34
	s_nop 1
	v_permlane16_swap_b32_e32 v34, v146
	v_add_f32_e32 v34, v34, v146
	v_mov_b32_e32 v146, v34
	s_nop 1
	v_permlane32_swap_b32_e32 v34, v146
	v_add_f32_e32 v34, v34, v146
	v_fmamk_f32 v34, v34, 0x3a000000, v135
	v_cmp_gt_f32_e32 vcc, s44, v34
	v_mul_f32_e32 v146, 0x4f800000, v34
	s_nop 0
	v_cndmask_b32_e32 v34, v34, v146, vcc
	v_sqrt_f32_e32 v146, v34
	s_nop 0
	v_add_u32_e32 v147, -1, v146
	v_fma_f32 v148, -v147, v146, v34
	v_cmp_ge_f32_e64 s[12:13], 0, v148
	v_add_u32_e32 v148, 1, v146
	s_nop 0
	v_cndmask_b32_e64 v147, v146, v147, s[12:13]
	v_fma_f32 v146, -v148, v146, v34
	v_cmp_lt_f32_e64 s[12:13], 0, v146
	s_nop 1
	v_cndmask_b32_e64 v146, v147, v148, s[12:13]
	v_mul_f32_e32 v147, 0x37800000, v146
	v_cndmask_b32_e32 v146, v146, v147, vcc
	v_cmp_class_f32_e32 vcc, v34, v136
	s_nop 1
	v_cndmask_b32_e32 v34, v146, v34, vcc
	v_div_scale_f32 v146, s[12:13], v34, v34, 1.0
	v_rcp_f32_e32 v147, v146
	s_nop 0
	v_fma_f32 v148, -v146, v147, 1.0
	v_fmac_f32_e32 v147, v148, v147
	v_div_scale_f32 v148, vcc, 1.0, v34, 1.0
	v_mul_f32_e32 v149, v148, v147
	v_fma_f32 v150, -v146, v149, v148
	v_fmac_f32_e32 v149, v150, v147
	v_fma_f32 v146, -v146, v149, v148
	v_div_fmas_f32 v146, v146, v147, v149
	v_div_fixup_f32 v34, v146, v34, 1.0
	v_pk_mul_f32 v[6:7], v[6:7], v[34:35] op_sel_hi:[1,0]
	v_pk_mul_f32 v[70:71], v[70:71], v[34:35] op_sel_hi:[1,0]
	v_pk_mul_f32 v[66:67], v[66:67], v[34:35] op_sel_hi:[1,0]
	v_pk_mul_f32 v[68:69], v[68:69], v[34:35] op_sel_hi:[1,0]
	v_pk_fma_f32 v[6:7], v[180:181], v[6:7], v[184:185]
	v_cvt_pk_fp8_f32 v244, v6, v7
	v_pk_fma_f32 v[70:71], v[182:183], v[70:71], v[186:187]
	v_lshl_add_u64 v[6:7], s[92:93], 0, v[2:3]
	v_lshl_add_u64 v[6:7], v[6:7], 0, v[178:179]
	v_pk_mul_f32 v[64:65], v[64:65], v[34:35] op_sel_hi:[1,0]
	v_cvt_pk_fp8_f32 v244, v70, v71 op_sel:[0,0,1]
	v_pk_mul_f32 v[62:63], v[62:63], v[34:35] op_sel_hi:[1,0]
	v_pk_mul_f32 v[58:59], v[58:59], v[34:35] op_sel_hi:[1,0]
	v_pk_mul_f32 v[60:61], v[60:61], v[34:35] op_sel_hi:[1,0]
	v_pk_mul_f32 v[56:57], v[56:57], v[34:35] op_sel_hi:[1,0]
	v_pk_mul_f32 v[54:55], v[54:55], v[34:35] op_sel_hi:[1,0]
	v_pk_mul_f32 v[32:33], v[32:33], v[34:35] op_sel_hi:[1,0]
	v_pk_fma_f32 v[66:67], v[188:189], v[66:67], v[192:193]
	v_pk_fma_f32 v[68:69], v[190:191], v[68:69], v[194:195]
	v_cvt_pk_fp8_f32 v245, v66, v67
	v_pk_mul_f32 v[52:53], v[52:53], v[34:35] op_sel_hi:[1,0]
	v_pk_mul_f32 v[30:31], v[30:31], v[34:35] op_sel_hi:[1,0]
	v_pk_mul_f32 v[28:29], v[28:29], v[34:35] op_sel_hi:[1,0]
	v_cvt_pk_fp8_f32 v245, v68, v69 op_sel:[0,0,1]
	v_pk_mul_f32 v[24:25], v[24:25], v[34:35] op_sel_hi:[1,0]
	v_pk_mul_f32 v[26:27], v[26:27], v[34:35] op_sel_hi:[1,0]
	v_pk_fma_f32 v[64:65], v[64:65], v[196:197], v[200:201]
	v_cvt_pk_fp8_f32 v246, v64, v65
	v_pk_fma_f32 v[62:63], v[62:63], v[198:199], v[202:203]
	s_nop 0
	v_cvt_pk_fp8_f32 v246, v62, v63 op_sel:[0,0,1]
	v_pk_fma_f32 v[58:59], v[58:59], v[204:205], v[208:209]
	v_cvt_pk_fp8_f32 v247, v58, v59
	v_pk_fma_f32 v[60:61], v[60:61], v[206:207], v[210:211]
	s_nop 0
	v_cvt_pk_fp8_f32 v247, v60, v61 op_sel:[0,0,1]
	s_nop 1
	s_mov_b32 vcc_lo, 0x55555555
	s_mov_b32 vcc_hi, 0x55555555
	v_cndmask_b32_dpp v252, v245, v244, vcc quad_perm:[1,0,3,2] row_mask:0xf bank_mask:0xf
	v_cndmask_b32_dpp v253, v247, v246, vcc quad_perm:[1,0,3,2] row_mask:0xf bank_mask:0xf
	s_mov_b32 vcc_lo, 0xaaaaaaaa
	s_mov_b32 vcc_hi, 0xaaaaaaaa
	v_cndmask_b32_dpp v245, v244, v245, vcc quad_perm:[1,0,3,2] row_mask:0xf bank_mask:0xf
	v_cndmask_b32_dpp v247, v246, v247, vcc quad_perm:[1,0,3,2] row_mask:0xf bank_mask:0xf
	s_mov_b32 vcc_lo, 0x33333333
	s_mov_b32 vcc_hi, 0x33333333
	v_cndmask_b32_dpp v248, v253, v252, vcc quad_perm:[2,3,0,1] row_mask:0xf bank_mask:0xf
	v_cndmask_b32_dpp v249, v247, v245, vcc quad_perm:[2,3,0,1] row_mask:0xf bank_mask:0xf
	s_mov_b32 vcc_lo, 0xcccccccc
	s_mov_b32 vcc_hi, 0xcccccccc
	v_cndmask_b32_dpp v250, v252, v253, vcc quad_perm:[2,3,0,1] row_mask:0xf bank_mask:0xf
	v_cndmask_b32_dpp v251, v245, v247, vcc quad_perm:[2,3,0,1] row_mask:0xf bank_mask:0xf
	global_store_dwordx4 v[6:7], v[248:251], off offset:-2048 sc0 sc1
	v_pk_fma_f32 v[56:57], v[56:57], v[212:213], v[216:217]
	v_cvt_pk_fp8_f32 v244, v56, v57
	v_pk_fma_f32 v[54:55], v[54:55], v[214:215], v[218:219]
	s_nop 0
	v_cvt_pk_fp8_f32 v244, v54, v55 op_sel:[0,0,1]
	v_pk_fma_f32 v[32:33], v[32:33], v[220:221], v[224:225]
	v_cvt_pk_fp8_f32 v245, v32, v33
	v_pk_fma_f32 v[52:53], v[52:53], v[222:223], v[226:227]
	v_cvt_pk_fp8_f32 v245, v52, v53 op_sel:[0,0,1]
	v_pk_fma_f32 v[30:31], v[30:31], v[228:229], v[232:233]
	s_nop 0
	v_cvt_pk_fp8_f32 v246, v30, v31
	v_pk_fma_f32 v[28:29], v[28:29], v[230:231], v[234:235]
	s_nop 0
	v_cvt_pk_fp8_f32 v246, v28, v29 op_sel:[0,0,1]
	v_pk_fma_f32 v[24:25], v[24:25], v[236:237], v[240:241]
	v_cvt_pk_fp8_f32 v247, v24, v25
	v_pk_fma_f32 v[26:27], v[26:27], v[238:239], v[242:243]
	s_nop 0
	v_cvt_pk_fp8_f32 v247, v26, v27 op_sel:[0,0,1]
	s_nop 1
	s_mov_b32 vcc_lo, 0x55555555
	s_mov_b32 vcc_hi, 0x55555555
	v_cndmask_b32_dpp v252, v245, v244, vcc quad_perm:[1,0,3,2] row_mask:0xf bank_mask:0xf
	v_cndmask_b32_dpp v253, v247, v246, vcc quad_perm:[1,0,3,2] row_mask:0xf bank_mask:0xf
	s_mov_b32 vcc_lo, 0xaaaaaaaa
	s_mov_b32 vcc_hi, 0xaaaaaaaa
	v_cndmask_b32_dpp v245, v244, v245, vcc quad_perm:[1,0,3,2] row_mask:0xf bank_mask:0xf
	v_cndmask_b32_dpp v247, v246, v247, vcc quad_perm:[1,0,3,2] row_mask:0xf bank_mask:0xf
	s_mov_b32 vcc_lo, 0x33333333
	s_mov_b32 vcc_hi, 0x33333333
	v_cndmask_b32_dpp v248, v253, v252, vcc quad_perm:[2,3,0,1] row_mask:0xf bank_mask:0xf
	v_cndmask_b32_dpp v249, v247, v245, vcc quad_perm:[2,3,0,1] row_mask:0xf bank_mask:0xf
	s_mov_b32 vcc_lo, 0xcccccccc
	s_mov_b32 vcc_hi, 0xcccccccc
	v_cndmask_b32_dpp v250, v252, v253, vcc quad_perm:[2,3,0,1] row_mask:0xf bank_mask:0xf
	v_cndmask_b32_dpp v251, v245, v247, vcc quad_perm:[2,3,0,1] row_mask:0xf bank_mask:0xf
	global_store_dwordx4 v[6:7], v[248:251], off offset:-1024 sc0 sc1
	s_and_saveexec_b64 s[12:13], s[8:9]
	s_cbranch_execz .LBB0_708
	s_add_i32 s70, s37, -8
	s_add_u32 s68, s92, s14
	v_mul_f32_e32 v24, 0x3a000000, v145
	s_addc_u32 s69, s93, s15
	v_mov_b32_e32 v25, v34
	v_mov_b32_e32 v26, s70
	ds_write_b64 v26, v[24:25]
	global_store_dwordx2 v137, v[24:25], s[68:69]
.LBB0_708:
	s_or_b64 exec, exec, s[12:13]
	s_waitcnt vmcnt(17)
	v_lshlrev_b32_e32 v58, 16, v22
	v_and_b32_e32 v59, 0xffff0000, v22
	v_lshlrev_b32_e32 v56, 16, v23
	v_and_b32_e32 v57, 0xffff0000, v23
	v_add_f32_e32 v22, v58, v59
	v_add_f32_e32 v23, v56, v57
	s_waitcnt vmcnt(16)
	v_lshlrev_b32_e32 v52, 16, v20
	v_and_b32_e32 v53, 0xffff0000, v20
	v_lshlrev_b32_e32 v54, 16, v21
	v_and_b32_e32 v55, 0xffff0000, v21
	v_add_f32_e32 v22, v22, v23
	v_add_f32_e32 v20, v52, v53
	v_add_f32_e32 v21, v54, v55
	s_waitcnt vmcnt(15)
	v_lshlrev_b32_e32 v32, 16, v18
	v_and_b32_e32 v33, 0xffff0000, v18
	v_lshlrev_b32_e32 v30, 16, v19
	v_and_b32_e32 v31, 0xffff0000, v19
	v_add_f32_e32 v22, 0, v22
	v_add_f32_e32 v20, v20, v21
	v_add_f32_e32 v18, v32, v33
	v_add_f32_e32 v19, v30, v31
	v_add_f32_e32 v20, v22, v20
	v_add_f32_e32 v18, v18, v19
	s_waitcnt vmcnt(14)
	v_lshlrev_b32_e32 v26, 16, v16
	v_and_b32_e32 v27, 0xffff0000, v16
	v_lshlrev_b32_e32 v28, 16, v17
	v_and_b32_e32 v29, 0xffff0000, v17
	v_add_f32_e32 v18, v20, v18
	v_add_f32_e32 v16, v26, v27
	v_add_f32_e32 v17, v28, v29
	s_waitcnt vmcnt(13)
	v_lshlrev_b32_e32 v22, 16, v14
	v_and_b32_e32 v23, 0xffff0000, v14
	v_lshlrev_b32_e32 v20, 16, v15
	v_and_b32_e32 v21, 0xffff0000, v15
	v_add_f32_e32 v16, v16, v17
	v_add_f32_e32 v14, v22, v23
	v_add_f32_e32 v15, v20, v21
	v_add_f32_e32 v16, v18, v16
	v_add_f32_e32 v14, v14, v15
	v_add_f32_e32 v14, v16, v14
	s_waitcnt vmcnt(12)
	v_lshlrev_b32_e32 v16, 16, v12
	v_and_b32_e32 v17, 0xffff0000, v12
	v_lshlrev_b32_e32 v18, 16, v13
	v_and_b32_e32 v19, 0xffff0000, v13
	v_add_f32_e32 v12, v16, v17
	v_add_f32_e32 v13, v18, v19
	v_add_f32_e32 v12, v12, v13
	v_add_f32_e32 v24, v14, v12
	s_waitcnt vmcnt(11)
	v_lshlrev_b32_e32 v14, 16, v10
	v_and_b32_e32 v15, 0xffff0000, v10
	v_lshlrev_b32_e32 v12, 16, v11
	v_and_b32_e32 v13, 0xffff0000, v11
	v_add_f32_e32 v10, v14, v15
	v_add_f32_e32 v11, v12, v13
	v_add_f32_e32 v10, v10, v11
	v_add_f32_e32 v24, v24, v10
	s_waitcnt vmcnt(10)
	v_lshlrev_b32_e32 v10, 16, v8
	v_and_b32_e32 v11, 0xffff0000, v8
	v_lshlrev_b32_e32 v8, 16, v9
	v_and_b32_e32 v9, 0xffff0000, v9
	v_add_f32_e32 v25, v10, v11
	v_add_f32_e32 v34, v8, v9
	v_add_f32_e32 v25, v25, v34
	v_add_f32_e32 v24, v24, v25
	s_nop 1
	v_add_f32_dpp v24, v24, v24 quad_perm:[1,0,3,2] row_mask:0xf bank_mask:0xf bound_ctrl:1
	s_nop 1
	v_add_f32_dpp v24, v24, v24 quad_perm:[2,3,0,1] row_mask:0xf bank_mask:0xf bound_ctrl:1
	s_nop 1
	v_add_f32_dpp v24, v24, v24 row_half_mirror row_mask:0xf bank_mask:0xf bound_ctrl:1
	s_nop 1
	v_add_f32_dpp v24, v24, v24 row_mirror row_mask:0xf bank_mask:0xf bound_ctrl:1
	v_mov_b32_e32 v25, v24
	s_nop 1
	v_permlane16_swap_b32_e32 v24, v25
	v_add_f32_e32 v24, v24, v25
	v_mov_b32_e32 v25, v24
	s_nop 1
	v_permlane32_swap_b32_e32 v24, v25
	v_add_f32_e32 v25, v24, v25
	v_fmac_f32_e32 v57, 0xba000000, v25
	v_fmac_f32_e32 v59, 0xba000000, v25
	v_fmac_f32_e32 v56, 0xba000000, v25
	v_fmac_f32_e32 v58, 0xba000000, v25
	v_mul_f32_e32 v24, v59, v59
	v_mul_f32_e32 v34, v57, v57
	v_fmac_f32_e32 v24, v58, v58
	v_fmac_f32_e32 v34, v56, v56
	v_fmac_f32_e32 v55, 0xba000000, v25
	v_fmac_f32_e32 v53, 0xba000000, v25
	v_add_f32_e32 v24, v24, v34
	v_fmac_f32_e32 v54, 0xba000000, v25
	v_fmac_f32_e32 v52, 0xba000000, v25
	v_mul_f32_e32 v34, v53, v53
	v_mul_f32_e32 v60, v55, v55
	v_fmac_f32_e32 v34, v52, v52
	v_fmac_f32_e32 v60, v54, v54
	v_add_f32_e32 v34, v34, v60
	v_fmac_f32_e32 v31, 0xba000000, v25
	v_fmac_f32_e32 v33, 0xba000000, v25
	v_add_f32_e32 v24, v24, v34
	v_fmac_f32_e32 v30, 0xba000000, v25
	v_fmac_f32_e32 v32, 0xba000000, v25
	v_mul_f32_e32 v34, v33, v33
	v_mul_f32_e32 v60, v31, v31
	v_fmac_f32_e32 v34, v32, v32
	v_fmac_f32_e32 v60, v30, v30
	v_add_f32_e32 v34, v34, v60
	v_fmac_f32_e32 v29, 0xba000000, v25
	v_fmac_f32_e32 v27, 0xba000000, v25
	v_add_f32_e32 v24, v34, v24
	v_fmac_f32_e32 v28, 0xba000000, v25
	v_fmac_f32_e32 v26, 0xba000000, v25
	v_mul_f32_e32 v34, v27, v27
	v_mul_f32_e32 v60, v29, v29
	v_fmac_f32_e32 v34, v26, v26
	v_fmac_f32_e32 v60, v28, v28
	v_add_f32_e32 v34, v34, v60
	v_fmac_f32_e32 v21, 0xba000000, v25
	v_fmac_f32_e32 v23, 0xba000000, v25
	v_add_f32_e32 v24, v34, v24
	v_fmac_f32_e32 v20, 0xba000000, v25
	v_fmac_f32_e32 v22, 0xba000000, v25
	v_mul_f32_e32 v34, v23, v23
	v_mul_f32_e32 v60, v21, v21
	v_fmac_f32_e32 v34, v22, v22
	v_fmac_f32_e32 v60, v20, v20
	v_add_f32_e32 v34, v34, v60
	v_fmac_f32_e32 v19, 0xba000000, v25
	v_fmac_f32_e32 v17, 0xba000000, v25
	v_add_f32_e32 v24, v34, v24
	v_fmac_f32_e32 v18, 0xba000000, v25
	v_fmac_f32_e32 v16, 0xba000000, v25
	v_mul_f32_e32 v34, v17, v17
	v_mul_f32_e32 v60, v19, v19
	v_fmac_f32_e32 v34, v16, v16
	v_fmac_f32_e32 v60, v18, v18
	v_add_f32_e32 v34, v34, v60
	v_fmac_f32_e32 v13, 0xba000000, v25
	v_fmac_f32_e32 v15, 0xba000000, v25
	v_add_f32_e32 v24, v34, v24
	v_fmac_f32_e32 v12, 0xba000000, v25
	v_fmac_f32_e32 v14, 0xba000000, v25
	v_mul_f32_e32 v34, v15, v15
	v_mul_f32_e32 v60, v13, v13
	v_fmac_f32_e32 v34, v14, v14
	v_fmac_f32_e32 v60, v12, v12
	v_add_f32_e32 v34, v34, v60
	v_fmac_f32_e32 v9, 0xba000000, v25
	v_fmac_f32_e32 v11, 0xba000000, v25
	v_add_f32_e32 v24, v34, v24
	v_fmac_f32_e32 v8, 0xba000000, v25
	v_fmac_f32_e32 v10, 0xba000000, v25
	v_mul_f32_e32 v34, v11, v11
	v_mul_f32_e32 v60, v9, v9
	v_fmac_f32_e32 v34, v10, v10
	v_fmac_f32_e32 v60, v8, v8
	v_add_f32_e32 v34, v34, v60
	v_add_f32_e32 v24, v34, v24
	s_nop 1
	v_add_f32_dpp v24, v24, v24 quad_perm:[1,0,3,2] row_mask:0xf bank_mask:0xf bound_ctrl:1
	s_nop 1
	v_add_f32_dpp v24, v24, v24 quad_perm:[2,3,0,1] row_mask:0xf bank_mask:0xf bound_ctrl:1
	s_nop 1
	v_add_f32_dpp v24, v24, v24 row_half_mirror row_mask:0xf bank_mask:0xf bound_ctrl:1
	s_nop 1
	v_add_f32_dpp v24, v24, v24 row_mirror row_mask:0xf bank_mask:0xf bound_ctrl:1
	v_mov_b32_e32 v34, v24
	s_nop 1
	v_permlane16_swap_b32_e32 v24, v34
	v_add_f32_e32 v24, v24, v34
	v_mov_b32_e32 v34, v24
	s_nop 1
	v_permlane32_swap_b32_e32 v24, v34
	v_add_f32_e32 v24, v24, v34
	v_fmamk_f32 v24, v24, 0x3a000000, v135
	v_cmp_gt_f32_e32 vcc, s44, v24
	v_mul_f32_e32 v34, 0x4f800000, v24
	s_nop 0
	v_cndmask_b32_e32 v24, v24, v34, vcc
	v_sqrt_f32_e32 v34, v24
	s_nop 0
	v_add_u32_e32 v60, -1, v34
	v_fma_f32 v61, -v60, v34, v24
	v_cmp_ge_f32_e64 s[12:13], 0, v61
	v_add_u32_e32 v61, 1, v34
	s_nop 0
	v_cndmask_b32_e64 v60, v34, v60, s[12:13]
	v_fma_f32 v34, -v61, v34, v24
	v_cmp_lt_f32_e64 s[12:13], 0, v34
	s_nop 1
	v_cndmask_b32_e64 v34, v60, v61, s[12:13]
	v_mul_f32_e32 v60, 0x37800000, v34
	v_cndmask_b32_e32 v34, v34, v60, vcc
	v_cmp_class_f32_e32 vcc, v24, v136
	s_nop 1
	v_cndmask_b32_e32 v24, v34, v24, vcc
	v_div_scale_f32 v34, s[12:13], v24, v24, 1.0
	v_rcp_f32_e32 v60, v34
	s_nop 0
	v_fma_f32 v61, -v34, v60, 1.0
	v_fmac_f32_e32 v60, v61, v60
	v_div_scale_f32 v61, vcc, 1.0, v24, 1.0
	v_mul_f32_e32 v62, v61, v60
	v_fma_f32 v63, -v34, v62, v61
	v_fmac_f32_e32 v62, v63, v60
	v_fma_f32 v34, -v34, v62, v61
	v_div_fmas_f32 v34, v34, v60, v62
	v_div_fixup_f32 v24, v34, v24, 1.0
	v_pk_mul_f32 v[58:59], v[58:59], v[24:25] op_sel_hi:[1,0]
	v_pk_mul_f32 v[56:57], v[56:57], v[24:25] op_sel_hi:[1,0]
	v_pk_fma_f32 v[58:59], v[180:181], v[58:59], v[184:185]
	v_pk_fma_f32 v[56:57], v[182:183], v[56:57], v[186:187]
	v_cvt_pk_fp8_f32 v244, v58, v59
	v_pk_mul_f32 v[52:53], v[52:53], v[24:25] op_sel_hi:[1,0]
	v_pk_mul_f32 v[54:55], v[54:55], v[24:25] op_sel_hi:[1,0]
	v_pk_mul_f32 v[32:33], v[32:33], v[24:25] op_sel_hi:[1,0]
	v_cvt_pk_fp8_f32 v244, v56, v57 op_sel:[0,0,1]
	v_pk_mul_f32 v[30:31], v[30:31], v[24:25] op_sel_hi:[1,0]
	v_pk_mul_f32 v[26:27], v[26:27], v[24:25] op_sel_hi:[1,0]
	v_pk_mul_f32 v[28:29], v[28:29], v[24:25] op_sel_hi:[1,0]
	v_pk_mul_f32 v[22:23], v[22:23], v[24:25] op_sel_hi:[1,0]
	v_pk_mul_f32 v[20:21], v[20:21], v[24:25] op_sel_hi:[1,0]
	v_pk_mul_f32 v[16:17], v[16:17], v[24:25] op_sel_hi:[1,0]
	v_pk_fma_f32 v[52:53], v[188:189], v[52:53], v[192:193]
	v_pk_fma_f32 v[54:55], v[190:191], v[54:55], v[194:195]
	v_cvt_pk_fp8_f32 v245, v52, v53
	v_pk_mul_f32 v[18:19], v[18:19], v[24:25] op_sel_hi:[1,0]
	v_pk_mul_f32 v[14:15], v[14:15], v[24:25] op_sel_hi:[1,0]
	v_pk_mul_f32 v[12:13], v[12:13], v[24:25] op_sel_hi:[1,0]
	v_cvt_pk_fp8_f32 v245, v54, v55 op_sel:[0,0,1]
	v_pk_mul_f32 v[10:11], v[10:11], v[24:25] op_sel_hi:[1,0]
	v_pk_mul_f32 v[8:9], v[8:9], v[24:25] op_sel_hi:[1,0]
	v_pk_fma_f32 v[32:33], v[32:33], v[196:197], v[200:201]
	s_nop 0
	v_cvt_pk_fp8_f32 v246, v32, v33
	v_pk_fma_f32 v[30:31], v[30:31], v[198:199], v[202:203]
	s_nop 0
	v_cvt_pk_fp8_f32 v246, v30, v31 op_sel:[0,0,1]
	v_pk_fma_f32 v[26:27], v[26:27], v[204:205], v[208:209]
	v_cvt_pk_fp8_f32 v247, v26, v27
	v_pk_fma_f32 v[28:29], v[28:29], v[206:207], v[210:211]
	s_nop 0
	v_cvt_pk_fp8_f32 v247, v28, v29 op_sel:[0,0,1]
	s_nop 1
	s_mov_b32 vcc_lo, 0x55555555
	s_mov_b32 vcc_hi, 0x55555555
	v_cndmask_b32_dpp v252, v245, v244, vcc quad_perm:[1,0,3,2] row_mask:0xf bank_mask:0xf
	v_cndmask_b32_dpp v253, v247, v246, vcc quad_perm:[1,0,3,2] row_mask:0xf bank_mask:0xf
	s_mov_b32 vcc_lo, 0xaaaaaaaa
	s_mov_b32 vcc_hi, 0xaaaaaaaa
	v_cndmask_b32_dpp v245, v244, v245, vcc quad_perm:[1,0,3,2] row_mask:0xf bank_mask:0xf
	v_cndmask_b32_dpp v247, v246, v247, vcc quad_perm:[1,0,3,2] row_mask:0xf bank_mask:0xf
	s_mov_b32 vcc_lo, 0x33333333
	s_mov_b32 vcc_hi, 0x33333333
	v_cndmask_b32_dpp v248, v253, v252, vcc quad_perm:[2,3,0,1] row_mask:0xf bank_mask:0xf
	v_cndmask_b32_dpp v249, v247, v245, vcc quad_perm:[2,3,0,1] row_mask:0xf bank_mask:0xf
	s_mov_b32 vcc_lo, 0xcccccccc
	s_mov_b32 vcc_hi, 0xcccccccc
	v_cndmask_b32_dpp v250, v252, v253, vcc quad_perm:[2,3,0,1] row_mask:0xf bank_mask:0xf
	v_cndmask_b32_dpp v251, v245, v247, vcc quad_perm:[2,3,0,1] row_mask:0xf bank_mask:0xf
	global_store_dwordx4 v[6:7], v[248:251], off sc0 sc1
	v_pk_fma_f32 v[22:23], v[22:23], v[212:213], v[216:217]
	v_cvt_pk_fp8_f32 v244, v22, v23
	v_pk_fma_f32 v[20:21], v[20:21], v[214:215], v[218:219]
	s_nop 0
	v_cvt_pk_fp8_f32 v244, v20, v21 op_sel:[0,0,1]
	v_pk_fma_f32 v[16:17], v[16:17], v[220:221], v[224:225]
	v_cvt_pk_fp8_f32 v245, v16, v17
	v_pk_fma_f32 v[18:19], v[18:19], v[222:223], v[226:227]
	s_nop 0
	v_cvt_pk_fp8_f32 v245, v18, v19 op_sel:[0,0,1]
	v_pk_fma_f32 v[14:15], v[14:15], v[228:229], v[232:233]
	v_cvt_pk_fp8_f32 v246, v14, v15
	v_pk_fma_f32 v[12:13], v[12:13], v[230:231], v[234:235]
	s_nop 0
	v_cvt_pk_fp8_f32 v246, v12, v13 op_sel:[0,0,1]
	v_pk_fma_f32 v[10:11], v[10:11], v[236:237], v[240:241]
	v_cvt_pk_fp8_f32 v247, v10, v11
	v_pk_fma_f32 v[8:9], v[8:9], v[238:239], v[242:243]
	s_nop 0
	v_cvt_pk_fp8_f32 v247, v8, v9 op_sel:[0,0,1]
	s_nop 1
	s_mov_b32 vcc_lo, 0x55555555
	s_mov_b32 vcc_hi, 0x55555555
	v_cndmask_b32_dpp v252, v245, v244, vcc quad_perm:[1,0,3,2] row_mask:0xf bank_mask:0xf
	v_cndmask_b32_dpp v253, v247, v246, vcc quad_perm:[1,0,3,2] row_mask:0xf bank_mask:0xf
	s_mov_b32 vcc_lo, 0xaaaaaaaa
	s_mov_b32 vcc_hi, 0xaaaaaaaa
	v_cndmask_b32_dpp v245, v244, v245, vcc quad_perm:[1,0,3,2] row_mask:0xf bank_mask:0xf
	v_cndmask_b32_dpp v247, v246, v247, vcc quad_perm:[1,0,3,2] row_mask:0xf bank_mask:0xf
	s_mov_b32 vcc_lo, 0x33333333
	s_mov_b32 vcc_hi, 0x33333333
	v_cndmask_b32_dpp v248, v253, v252, vcc quad_perm:[2,3,0,1] row_mask:0xf bank_mask:0xf
	v_cndmask_b32_dpp v249, v247, v245, vcc quad_perm:[2,3,0,1] row_mask:0xf bank_mask:0xf
	s_mov_b32 vcc_lo, 0xcccccccc
	s_mov_b32 vcc_hi, 0xcccccccc
	v_cndmask_b32_dpp v250, v252, v253, vcc quad_perm:[2,3,0,1] row_mask:0xf bank_mask:0xf
	v_cndmask_b32_dpp v251, v245, v247, vcc quad_perm:[2,3,0,1] row_mask:0xf bank_mask:0xf
	global_store_dwordx4 v[6:7], v[248:251], off offset:1024 sc0 sc1
	s_and_saveexec_b64 s[12:13], s[8:9]
	s_cbranch_execz .LBB0_705
	s_add_u32 s68, s92, s14
	v_mul_f32_e32 v6, 0x3a000000, v25
	s_addc_u32 s69, s93, s15
	v_mov_b32_e32 v7, v24
	v_mov_b32_e32 v8, s37
	ds_write_b64 v8, v[6:7]
	global_store_dwordx2 v137, v[6:7], s[68:69] offset:8
	s_branch .LBB0_705
